# v69 + P4 bisection without per-key VALU->SGPR traffic: bit 31 first, 31-bit keys, sign-bit history (v_alignbit) + popcount + DPP wave sum
# baseline (speedup 1.0000x reference)
; #define SEL_ROW(idx, row, nv) const int bb_ = (idx) >> 11; int t_ = (idx) & 2047; if (bb_ & 1) t_ = 2047 - t_; const size_t row = (size_t)bb_ * SEQ + t_; const int nv = (t_ >> 6) + 1;
; __device__ __forceinline__ void ph4b_body(const Args& a, int wave, int lane, int G, int bid) {
;     ...
;         SEL_ROW(idx, row, nv)
; #pragma unroll
;         for (int i = 0; i < 32; ++i) { const unsigned uu = __float_as_uint(raw[i]); const unsigned kk = (uu & 0x80000000u) ? ~uu : (uu | 0x80000000u); key[i] = (i < nv) ? kk : 0u; }
;         if (idx + NGW < T) { SEL_ROW(idx + NGW, rown, nvn) const float* sp = SC + rown * 2048 + lane;
; #pragma unroll
;             for (int i = 0; i < 32; ++i) raw[i] = __builtin_nontemporal_load(sp + 64 * (i < nvn ? i : nvn - 1)); }
;         unsigned Tt = 0u;
;         if (nv > 4) { if (nv <= 8) Tt = sel_thr<8>(key); else if (nv <= 16) Tt = sel_thr<16>(key); else if (nv <= 24) Tt = sel_thr<24>(key); else Tt = sel_thr<32>(key); }
.LBB0_700:
	s_and_b32 s0, s33, 0x7ff
	v_not_b32_e32 v5, v66
	v_cmp_gt_i32_e32 vcc, 0, v66
	s_and_b32 s1, s33, 0x800
	s_xor_b32 s2, s0, 0x7ff
	v_cndmask_b32_e64 v5, -|v66|, v5, vcc
	v_not_b32_e32 v66, v36
	v_cmp_gt_i32_e32 vcc, 0, v36
	s_cmp_eq_u32 s1, 0
	s_cselect_b32 s34, s0, s2
	v_cndmask_b32_e64 v36, -|v36|, v66, vcc
	v_not_b32_e32 v66, v37
	v_cmp_gt_i32_e32 vcc, 0, v37
	s_lshr_b32 s38, s34, 6
	s_cmpk_gt_u32 s34, 0x13f
	v_cndmask_b32_e64 v37, -|v37|, v66, vcc
	v_not_b32_e32 v66, v38
	v_cmp_gt_i32_e32 vcc, 0, v38
	s_nop 1
	v_cndmask_b32_e64 v38, -|v38|, v66, vcc
	v_not_b32_e32 v66, v39
	v_cmp_gt_i32_e32 vcc, 0, v39
	s_nop 1
	v_cndmask_b32_e64 v39, -|v39|, v66, vcc
	v_not_b32_e32 v66, v35
	v_cmp_gt_i32_e32 vcc, 0, v35
	s_nop 1
	v_cndmask_b32_e64 v67, -|v35|, v66, vcc
	s_cselect_b64 vcc, -1, 0
	v_cndmask_b32_e32 v35, 0, v67, vcc
	v_not_b32_e32 v66, v40
	v_cmp_gt_i32_e32 vcc, 0, v40
	s_cmpk_gt_u32 s34, 0x17f
	s_nop 0
	v_cndmask_b32_e64 v68, -|v40|, v66, vcc
	s_cselect_b64 vcc, -1, 0
	v_cndmask_b32_e32 v40, 0, v68, vcc
	v_not_b32_e32 v66, v41
	v_cmp_gt_i32_e32 vcc, 0, v41
	s_cmpk_gt_u32 s34, 0x1bf
	s_nop 0
	v_cndmask_b32_e64 v69, -|v41|, v66, vcc
	s_cselect_b64 vcc, -1, 0
	s_cmpk_lt_u32 s34, 0x200
	v_cndmask_b32_e32 v41, 0, v69, vcc
	v_not_b32_e32 v66, v43
	v_cmp_gt_i32_e32 vcc, 0, v43
	s_cselect_b64 s[0:1], -1, 0
	s_cmpk_gt_u32 s34, 0x1ff
	v_cndmask_b32_e64 v43, -|v43|, v66, vcc
	s_cselect_b64 s[6:7], -1, 0
	v_not_b32_e32 v66, v42
	v_cmp_gt_i32_e32 vcc, 0, v42
	s_cmpk_gt_u32 s34, 0x23f
	s_nop 0
	v_cndmask_b32_e64 v70, -|v42|, v66, vcc
	s_cselect_b64 vcc, -1, 0
	v_cndmask_b32_e32 v42, 0, v70, vcc
	v_not_b32_e32 v66, v44
	v_cmp_gt_i32_e32 vcc, 0, v44
	s_cmpk_gt_u32 s34, 0x27f
	s_nop 0
	v_cndmask_b32_e64 v71, -|v44|, v66, vcc
	s_cselect_b64 vcc, -1, 0
	v_cndmask_b32_e32 v44, 0, v71, vcc
	v_not_b32_e32 v66, v45
	v_cmp_gt_i32_e32 vcc, 0, v45
	s_cmpk_gt_u32 s34, 0x2bf
	s_nop 0
	v_cndmask_b32_e64 v72, -|v45|, v66, vcc
	s_cselect_b64 vcc, -1, 0
	v_cndmask_b32_e32 v45, 0, v72, vcc
	v_not_b32_e32 v66, v46
	v_cmp_gt_i32_e32 vcc, 0, v46
	s_cmpk_gt_u32 s34, 0x2ff
	s_nop 0
	v_cndmask_b32_e64 v73, -|v46|, v66, vcc
	s_cselect_b64 vcc, -1, 0
	v_cndmask_b32_e32 v46, 0, v73, vcc
	v_not_b32_e32 v66, v47
	v_cmp_gt_i32_e32 vcc, 0, v47
	s_cmpk_gt_u32 s34, 0x33f
	s_nop 0
	v_cndmask_b32_e64 v74, -|v47|, v66, vcc
	s_cselect_b64 vcc, -1, 0
	v_cndmask_b32_e32 v47, 0, v74, vcc
	v_not_b32_e32 v66, v48
	v_cmp_gt_i32_e32 vcc, 0, v48
	s_cmpk_gt_u32 s34, 0x37f
	s_nop 0
	v_cndmask_b32_e64 v75, -|v48|, v66, vcc
	s_cselect_b64 vcc, -1, 0
	v_cndmask_b32_e32 v48, 0, v75, vcc
	v_not_b32_e32 v66, v49
	v_cmp_gt_i32_e32 vcc, 0, v49
	s_cmpk_gt_u32 s34, 0x3bf
	s_nop 0
	v_cndmask_b32_e64 v76, -|v49|, v66, vcc
	s_cselect_b64 vcc, -1, 0
	s_cmpk_lt_u32 s34, 0x400
	v_cndmask_b32_e32 v49, 0, v76, vcc
	v_not_b32_e32 v66, v52
	v_cmp_gt_i32_e32 vcc, 0, v52
	s_cselect_b64 s[2:3], -1, 0
	s_cmpk_gt_u32 s34, 0x3ff
	v_cndmask_b32_e64 v52, -|v52|, v66, vcc
	s_cselect_b64 s[8:9], -1, 0
	v_not_b32_e32 v66, v50
	v_cmp_gt_i32_e32 vcc, 0, v50
	s_cmpk_gt_u32 s34, 0x43f
	s_nop 0
	v_cndmask_b32_e64 v77, -|v50|, v66, vcc
	s_cselect_b64 vcc, -1, 0
	v_cndmask_b32_e32 v50, 0, v77, vcc
	v_not_b32_e32 v66, v51
	v_cmp_gt_i32_e32 vcc, 0, v51
	s_cmpk_gt_u32 s34, 0x47f
	s_nop 0
	v_cndmask_b32_e64 v78, -|v51|, v66, vcc
	s_cselect_b64 vcc, -1, 0
	v_cndmask_b32_e32 v51, 0, v78, vcc
	v_not_b32_e32 v66, v53
	v_cmp_gt_i32_e32 vcc, 0, v53
	s_cmpk_gt_u32 s34, 0x4bf
	s_nop 0
	v_cndmask_b32_e64 v79, -|v53|, v66, vcc
	s_cselect_b64 vcc, -1, 0
	v_cndmask_b32_e32 v53, 0, v79, vcc
	v_not_b32_e32 v66, v54
	v_cmp_gt_i32_e32 vcc, 0, v54
	s_cmpk_gt_u32 s34, 0x4ff
	s_nop 0
	v_cndmask_b32_e64 v80, -|v54|, v66, vcc
	s_cselect_b64 vcc, -1, 0
	v_cndmask_b32_e32 v54, 0, v80, vcc
	v_not_b32_e32 v66, v55
	v_cmp_gt_i32_e32 vcc, 0, v55
	s_cmpk_gt_u32 s34, 0x53f
	s_nop 0
	v_cndmask_b32_e64 v81, -|v55|, v66, vcc
	s_cselect_b64 vcc, -1, 0
	v_cndmask_b32_e32 v55, 0, v81, vcc
	v_not_b32_e32 v66, v56
	v_cmp_gt_i32_e32 vcc, 0, v56
	s_cmpk_gt_u32 s34, 0x57f
	s_nop 0
	v_cndmask_b32_e64 v82, -|v56|, v66, vcc
	s_cselect_b64 vcc, -1, 0
	v_cndmask_b32_e32 v56, 0, v82, vcc
	v_not_b32_e32 v66, v57
	v_cmp_gt_i32_e32 vcc, 0, v57
	s_cmpk_gt_u32 s34, 0x5bf
	s_nop 0
	v_cndmask_b32_e64 v83, -|v57|, v66, vcc
	s_cselect_b64 vcc, -1, 0
	s_cmpk_lt_u32 s34, 0x600
	v_cndmask_b32_e32 v57, 0, v83, vcc
	v_not_b32_e32 v66, v62
	v_cmp_gt_i32_e32 vcc, 0, v62
	s_cselect_b64 s[4:5], -1, 0
	s_cmpk_gt_u32 s34, 0x5ff
	v_cndmask_b32_e64 v62, -|v62|, v66, vcc
	s_cselect_b64 s[10:11], -1, 0
	v_not_b32_e32 v66, v58
	v_cmp_gt_i32_e32 vcc, 0, v58
	s_cmpk_gt_u32 s34, 0x63f
	s_nop 0
	v_cndmask_b32_e64 v58, -|v58|, v66, vcc
	s_cselect_b64 vcc, -1, 0
	v_cndmask_b32_e32 v58, 0, v58, vcc
	v_not_b32_e32 v66, v59
	v_cmp_gt_i32_e32 vcc, 0, v59
	s_cmpk_gt_u32 s34, 0x67f
	s_nop 0
	v_cndmask_b32_e64 v59, -|v59|, v66, vcc
	s_cselect_b64 vcc, -1, 0
	v_cndmask_b32_e32 v59, 0, v59, vcc
	v_not_b32_e32 v66, v60
	v_cmp_gt_i32_e32 vcc, 0, v60
	s_cmpk_gt_u32 s34, 0x6bf
	s_nop 0
	v_cndmask_b32_e64 v60, -|v60|, v66, vcc
	s_cselect_b64 vcc, -1, 0
	v_cndmask_b32_e32 v60, 0, v60, vcc
	v_not_b32_e32 v66, v61
	v_cmp_gt_i32_e32 vcc, 0, v61
	s_cmpk_gt_u32 s34, 0x6ff
	s_nop 0
	v_cndmask_b32_e64 v61, -|v61|, v66, vcc
	s_cselect_b64 vcc, -1, 0
	v_cndmask_b32_e32 v61, 0, v61, vcc
	v_not_b32_e32 v66, v63
	v_cmp_gt_i32_e32 vcc, 0, v63
	s_cmpk_gt_u32 s34, 0x73f
	s_nop 0
	v_cndmask_b32_e64 v63, -|v63|, v66, vcc
	s_cselect_b64 vcc, -1, 0
	v_cndmask_b32_e32 v63, 0, v63, vcc
	v_not_b32_e32 v66, v64
	v_cmp_gt_i32_e32 vcc, 0, v64
	s_cmpk_gt_u32 s34, 0x77f
	s_nop 0
	v_cndmask_b32_e64 v64, -|v64|, v66, vcc
	s_cselect_b64 vcc, -1, 0
	v_cndmask_b32_e32 v64, 0, v64, vcc
	v_not_b32_e32 v66, v65
	v_cmp_gt_i32_e32 vcc, 0, v65
	s_cmp_eq_u32 s38, 31
	s_nop 0
	v_cndmask_b32_e64 v65, -|v65|, v66, vcc
	s_cselect_b64 vcc, -1, 0
	v_cndmask_b32_e32 v65, 0, v65, vcc
	s_cmpk_lt_u32 s34, 0x100
	v_mov_b32_e32 v66, 0
	s_cbranch_scc1 .LBB0_718
; template <int NVM> __device__ __forceinline__ int cnt_ge(const unsigned (&key)[32], unsigned cand) {
;     unsigned c0 = 0, c1 = 0, c2 = 0, c3 = 0;
; #pragma unroll
;     for (int i = 0; i < NVM; i += 4) {
;         asm("v_cmp_ge_u32 vcc, %1, %2\n\tv_addc_co_u32 %0, vcc, 0, %0, vcc" : "+v"(c0) : "v"(key[i]), "v"(cand) : "vcc");
;         asm("v_cmp_ge_u32 vcc, %1, %2\n\tv_addc_co_u32 %0, vcc, 0, %0, vcc" : "+v"(c1) : "v"(key[i + 1]), "v"(cand) : "vcc");
;         asm("v_cmp_ge_u32 vcc, %1, %2\n\tv_addc_co_u32 %0, vcc, 0, %0, vcc" : "+v"(c2) : "v"(key[i + 2]), "v"(cand) : "vcc");
;         asm("v_cmp_ge_u32 vcc, %1, %2\n\tv_addc_co_u32 %0, vcc, 0, %0, vcc" : "+v"(c3) : "v"(key[i + 3]), "v"(cand) : "vcc"); }
;     const unsigned c = (c0 + c1) + (c2 + c3);
;     int tot = 0;
; #pragma unroll
;     for (int b = 0; b < 6; ++b) tot += __builtin_popcountll(__ballot((c >> b) & 1u)) << b;
;     return tot;
; }
; template <int NVM> __device__ __forceinline__ unsigned sel_thr(const unsigned (&key)[32]) {
;     unsigned Tt = 0u;
;     ...
;         if (cnt >= TOPK) { Tt = cand; if (cnt == TOPK) break; } }
;     return Tt;
; }
	s_and_b64 vcc, exec, s[6:7]
	s_cbranch_vccz .LBB0_707
	s_and_b64 vcc, exec, s[8:9]
	s_cbranch_vccz .LBB0_708
	s_andn2_b64 vcc, exec, s[10:11]
	s_cbranch_vccnz .LBB0_709
	v_mov_b32_e32 v84, 31
	v_mov_b32_e32 v66, 0
	v_mov_b32_e32 v86, 0
	v_alignbit_b32 v86, v86, v5, 31
	v_alignbit_b32 v86, v86, v36, 31
	v_alignbit_b32 v86, v86, v39, 31
	v_alignbit_b32 v86, v86, v37, 31
	v_alignbit_b32 v86, v86, v38, 31
	v_alignbit_b32 v86, v86, v67, 31
	v_alignbit_b32 v86, v86, v43, 31
	v_alignbit_b32 v86, v86, v68, 31
	v_alignbit_b32 v86, v86, v69, 31
	v_alignbit_b32 v86, v86, v70, 31
	v_alignbit_b32 v86, v86, v73, 31
	v_alignbit_b32 v86, v86, v71, 31
	v_alignbit_b32 v86, v86, v72, 31
	v_alignbit_b32 v86, v86, v74, 31
	v_alignbit_b32 v86, v86, v52, 31
	v_alignbit_b32 v86, v86, v75, 31
	v_alignbit_b32 v86, v86, v76, 31
	v_alignbit_b32 v86, v86, v77, 31
	v_alignbit_b32 v86, v86, v80, 31
	v_alignbit_b32 v86, v86, v78, 31
	v_alignbit_b32 v86, v86, v79, 31
	v_alignbit_b32 v86, v86, v81, 31
	v_alignbit_b32 v86, v86, v62, 31
	v_alignbit_b32 v86, v86, v82, 31
	v_alignbit_b32 v86, v86, v83, 31
	v_alignbit_b32 v86, v86, v58, 31
	v_alignbit_b32 v86, v86, v61, 31
	v_alignbit_b32 v86, v86, v59, 31
	v_alignbit_b32 v86, v86, v60, 31
	v_alignbit_b32 v86, v86, v63, 31
	v_alignbit_b32 v86, v86, v64, 31
	v_alignbit_b32 v86, v86, v65, 31
	v_bcnt_u32_b32 v86, v86, 0
	s_nop 1
	v_add_u32_dpp v86, v86, v86 quad_perm:[1,0,3,2] row_mask:0xf bank_mask:0xf
	s_nop 1
	v_add_u32_dpp v86, v86, v86 quad_perm:[2,3,0,1] row_mask:0xf bank_mask:0xf
	s_nop 1
	v_add_u32_dpp v86, v86, v86 row_ror:4 row_mask:0xf bank_mask:0xf
	s_nop 1
	v_add_u32_dpp v86, v86, v86 row_ror:8 row_mask:0xf bank_mask:0xf
	s_nop 1
	v_add_u32_dpp v86, v86, v86 row_bcast:15 row_mask:0xa bank_mask:0xf
	s_nop 1
	v_add_u32_dpp v86, v86, v86 row_bcast:31 row_mask:0xc bank_mask:0xf
	s_nop 1
	v_readlane_b32 s12, v86, 63
	s_mov_b32 s28, 0
	s_mov_b32 s29, 0
	s_cmpk_lt_u32 s12, 0x100
	s_cbranch_scc1 .Lp4s_705_lo
	s_mov_b32 s29, 0x80000000
	s_cmpk_eq_u32 s12, 0x100
	s_cbranch_scc1 .Lp4s_705_done
	v_ashrrev_i32_e32 v88, 31, v5
	v_and_b32_e32 v89, 0x7fffffff, v5
	v_and_b32_e32 v200, v88, v89
	v_ashrrev_i32_e32 v88, 31, v36
	v_and_b32_e32 v89, 0x7fffffff, v36
	v_and_b32_e32 v201, v88, v89
	v_ashrrev_i32_e32 v88, 31, v39
	v_and_b32_e32 v89, 0x7fffffff, v39
	v_and_b32_e32 v202, v88, v89
	v_ashrrev_i32_e32 v88, 31, v37
	v_and_b32_e32 v89, 0x7fffffff, v37
	v_and_b32_e32 v203, v88, v89
	v_ashrrev_i32_e32 v88, 31, v38
	v_and_b32_e32 v89, 0x7fffffff, v38
	v_and_b32_e32 v204, v88, v89
	v_ashrrev_i32_e32 v88, 31, v67
	v_and_b32_e32 v89, 0x7fffffff, v67
	v_and_b32_e32 v205, v88, v89
	v_ashrrev_i32_e32 v88, 31, v43
	v_and_b32_e32 v89, 0x7fffffff, v43
	v_and_b32_e32 v206, v88, v89
	v_ashrrev_i32_e32 v88, 31, v68
	v_and_b32_e32 v89, 0x7fffffff, v68
	v_and_b32_e32 v207, v88, v89
	v_ashrrev_i32_e32 v88, 31, v69
	v_and_b32_e32 v89, 0x7fffffff, v69
	v_and_b32_e32 v208, v88, v89
	v_ashrrev_i32_e32 v88, 31, v70
	v_and_b32_e32 v89, 0x7fffffff, v70
	v_and_b32_e32 v209, v88, v89
	v_ashrrev_i32_e32 v88, 31, v73
	v_and_b32_e32 v89, 0x7fffffff, v73
	v_and_b32_e32 v210, v88, v89
	v_ashrrev_i32_e32 v88, 31, v71
	v_and_b32_e32 v89, 0x7fffffff, v71
	v_and_b32_e32 v211, v88, v89
	v_ashrrev_i32_e32 v88, 31, v72
	v_and_b32_e32 v89, 0x7fffffff, v72
	v_and_b32_e32 v212, v88, v89
	v_ashrrev_i32_e32 v88, 31, v74
	v_and_b32_e32 v89, 0x7fffffff, v74
	v_and_b32_e32 v213, v88, v89
	v_ashrrev_i32_e32 v88, 31, v52
	v_and_b32_e32 v89, 0x7fffffff, v52
	v_and_b32_e32 v214, v88, v89
	v_ashrrev_i32_e32 v88, 31, v75
	v_and_b32_e32 v89, 0x7fffffff, v75
	v_and_b32_e32 v215, v88, v89
	v_ashrrev_i32_e32 v88, 31, v76
	v_and_b32_e32 v89, 0x7fffffff, v76
	v_and_b32_e32 v216, v88, v89
	v_ashrrev_i32_e32 v88, 31, v77
	v_and_b32_e32 v89, 0x7fffffff, v77
	v_and_b32_e32 v217, v88, v89
	v_ashrrev_i32_e32 v88, 31, v80
	v_and_b32_e32 v89, 0x7fffffff, v80
	v_and_b32_e32 v218, v88, v89
	v_ashrrev_i32_e32 v88, 31, v78
	v_and_b32_e32 v89, 0x7fffffff, v78
	v_and_b32_e32 v219, v88, v89
	v_ashrrev_i32_e32 v88, 31, v79
	v_and_b32_e32 v89, 0x7fffffff, v79
	v_and_b32_e32 v220, v88, v89
	v_ashrrev_i32_e32 v88, 31, v81
	v_and_b32_e32 v89, 0x7fffffff, v81
	v_and_b32_e32 v221, v88, v89
	v_ashrrev_i32_e32 v88, 31, v62
	v_and_b32_e32 v89, 0x7fffffff, v62
	v_and_b32_e32 v222, v88, v89
	v_ashrrev_i32_e32 v88, 31, v82
	v_and_b32_e32 v89, 0x7fffffff, v82
	v_and_b32_e32 v223, v88, v89
	v_ashrrev_i32_e32 v88, 31, v83
	v_and_b32_e32 v89, 0x7fffffff, v83
	v_and_b32_e32 v224, v88, v89
	v_ashrrev_i32_e32 v88, 31, v58
	v_and_b32_e32 v89, 0x7fffffff, v58
	v_and_b32_e32 v225, v88, v89
	v_ashrrev_i32_e32 v88, 31, v61
	v_and_b32_e32 v89, 0x7fffffff, v61
	v_and_b32_e32 v226, v88, v89
	v_ashrrev_i32_e32 v88, 31, v59
	v_and_b32_e32 v89, 0x7fffffff, v59
	v_and_b32_e32 v227, v88, v89
	v_ashrrev_i32_e32 v88, 31, v60
	v_and_b32_e32 v89, 0x7fffffff, v60
	v_and_b32_e32 v228, v88, v89
	v_ashrrev_i32_e32 v88, 31, v63
	v_and_b32_e32 v89, 0x7fffffff, v63
	v_and_b32_e32 v229, v88, v89
	v_ashrrev_i32_e32 v88, 31, v64
	v_and_b32_e32 v89, 0x7fffffff, v64
	v_and_b32_e32 v230, v88, v89
	v_ashrrev_i32_e32 v88, 31, v65
	v_and_b32_e32 v89, 0x7fffffff, v65
	v_and_b32_e32 v231, v88, v89
	s_branch .Lp4s_705_go
; template <int NVM> __device__ __forceinline__ int cnt_ge(const unsigned (&key)[32], unsigned cand) {
;     unsigned c0 = 0, c1 = 0, c2 = 0, c3 = 0;
; #pragma unroll
;     for (int i = 0; i < NVM; i += 4) {
;         asm("v_cmp_ge_u32 vcc, %1, %2\n\tv_addc_co_u32 %0, vcc, 0, %0, vcc" : "+v"(c0) : "v"(key[i]), "v"(cand) : "vcc");
;         asm("v_cmp_ge_u32 vcc, %1, %2\n\tv_addc_co_u32 %0, vcc, 0, %0, vcc" : "+v"(c1) : "v"(key[i + 1]), "v"(cand) : "vcc");
;         asm("v_cmp_ge_u32 vcc, %1, %2\n\tv_addc_co_u32 %0, vcc, 0, %0, vcc" : "+v"(c2) : "v"(key[i + 2]), "v"(cand) : "vcc");
;         asm("v_cmp_ge_u32 vcc, %1, %2\n\tv_addc_co_u32 %0, vcc, 0, %0, vcc" : "+v"(c3) : "v"(key[i + 3]), "v"(cand) : "vcc"); }
;     const unsigned c = (c0 + c1) + (c2 + c3);
;     int tot = 0;
; #pragma unroll
;     for (int b = 0; b < 6; ++b) tot += __builtin_popcountll(__ballot((c >> b) & 1u)) << b;
;     return tot;
; }
; template <int NVM> __device__ __forceinline__ unsigned sel_thr(const unsigned (&key)[32]) {
;     unsigned Tt = 0u;
;     ...
;         if (cnt >= TOPK) { Tt = cand; if (cnt == TOPK) break; } }
;     return Tt;
; }
.Lp4s_705_lo:
	v_ashrrev_i32_e32 v88, 31, v5
	v_or_b32_e32 v89, v88, v5
	v_and_b32_e32 v200, 0x7fffffff, v89
	v_ashrrev_i32_e32 v88, 31, v36
	v_or_b32_e32 v89, v88, v36
	v_and_b32_e32 v201, 0x7fffffff, v89
	v_ashrrev_i32_e32 v88, 31, v39
	v_or_b32_e32 v89, v88, v39
	v_and_b32_e32 v202, 0x7fffffff, v89
	v_ashrrev_i32_e32 v88, 31, v37
	v_or_b32_e32 v89, v88, v37
	v_and_b32_e32 v203, 0x7fffffff, v89
	v_ashrrev_i32_e32 v88, 31, v38
	v_or_b32_e32 v89, v88, v38
	v_and_b32_e32 v204, 0x7fffffff, v89
	v_ashrrev_i32_e32 v88, 31, v67
	v_or_b32_e32 v89, v88, v67
	v_and_b32_e32 v205, 0x7fffffff, v89
	v_ashrrev_i32_e32 v88, 31, v43
	v_or_b32_e32 v89, v88, v43
	v_and_b32_e32 v206, 0x7fffffff, v89
	v_ashrrev_i32_e32 v88, 31, v68
	v_or_b32_e32 v89, v88, v68
	v_and_b32_e32 v207, 0x7fffffff, v89
	v_ashrrev_i32_e32 v88, 31, v69
	v_or_b32_e32 v89, v88, v69
	v_and_b32_e32 v208, 0x7fffffff, v89
	v_ashrrev_i32_e32 v88, 31, v70
	v_or_b32_e32 v89, v88, v70
	v_and_b32_e32 v209, 0x7fffffff, v89
	v_ashrrev_i32_e32 v88, 31, v73
	v_or_b32_e32 v89, v88, v73
	v_and_b32_e32 v210, 0x7fffffff, v89
	v_ashrrev_i32_e32 v88, 31, v71
	v_or_b32_e32 v89, v88, v71
	v_and_b32_e32 v211, 0x7fffffff, v89
	v_ashrrev_i32_e32 v88, 31, v72
	v_or_b32_e32 v89, v88, v72
	v_and_b32_e32 v212, 0x7fffffff, v89
	v_ashrrev_i32_e32 v88, 31, v74
	v_or_b32_e32 v89, v88, v74
	v_and_b32_e32 v213, 0x7fffffff, v89
	v_ashrrev_i32_e32 v88, 31, v52
	v_or_b32_e32 v89, v88, v52
	v_and_b32_e32 v214, 0x7fffffff, v89
	v_ashrrev_i32_e32 v88, 31, v75
	v_or_b32_e32 v89, v88, v75
	v_and_b32_e32 v215, 0x7fffffff, v89
	v_ashrrev_i32_e32 v88, 31, v76
	v_or_b32_e32 v89, v88, v76
	v_and_b32_e32 v216, 0x7fffffff, v89
	v_ashrrev_i32_e32 v88, 31, v77
	v_or_b32_e32 v89, v88, v77
	v_and_b32_e32 v217, 0x7fffffff, v89
	v_ashrrev_i32_e32 v88, 31, v80
	v_or_b32_e32 v89, v88, v80
	v_and_b32_e32 v218, 0x7fffffff, v89
	v_ashrrev_i32_e32 v88, 31, v78
	v_or_b32_e32 v89, v88, v78
	v_and_b32_e32 v219, 0x7fffffff, v89
	v_ashrrev_i32_e32 v88, 31, v79
	v_or_b32_e32 v89, v88, v79
	v_and_b32_e32 v220, 0x7fffffff, v89
	v_ashrrev_i32_e32 v88, 31, v81
	v_or_b32_e32 v89, v88, v81
	v_and_b32_e32 v221, 0x7fffffff, v89
	v_ashrrev_i32_e32 v88, 31, v62
	v_or_b32_e32 v89, v88, v62
	v_and_b32_e32 v222, 0x7fffffff, v89
	v_ashrrev_i32_e32 v88, 31, v82
	v_or_b32_e32 v89, v88, v82
	v_and_b32_e32 v223, 0x7fffffff, v89
	v_ashrrev_i32_e32 v88, 31, v83
	v_or_b32_e32 v89, v88, v83
	v_and_b32_e32 v224, 0x7fffffff, v89
	v_ashrrev_i32_e32 v88, 31, v58
	v_or_b32_e32 v89, v88, v58
	v_and_b32_e32 v225, 0x7fffffff, v89
	v_ashrrev_i32_e32 v88, 31, v61
	v_or_b32_e32 v89, v88, v61
	v_and_b32_e32 v226, 0x7fffffff, v89
	v_ashrrev_i32_e32 v88, 31, v59
	v_or_b32_e32 v89, v88, v59
	v_and_b32_e32 v227, 0x7fffffff, v89
	v_ashrrev_i32_e32 v88, 31, v60
	v_or_b32_e32 v89, v88, v60
	v_and_b32_e32 v228, 0x7fffffff, v89
	v_ashrrev_i32_e32 v88, 31, v63
	v_or_b32_e32 v89, v88, v63
	v_and_b32_e32 v229, 0x7fffffff, v89
	v_ashrrev_i32_e32 v88, 31, v64
	v_or_b32_e32 v89, v88, v64
	v_and_b32_e32 v230, 0x7fffffff, v89
	v_ashrrev_i32_e32 v88, 31, v65
	v_or_b32_e32 v89, v88, v65
	v_and_b32_e32 v231, 0x7fffffff, v89
.Lp4s_705_go:
	s_mov_b32 s26, 30
.LBB0_705:
	s_lshl_b32 s27, 1, s26
	s_or_b32 s27, s27, s28
	v_mov_b32_e32 v86, 0
	v_subrev_u32_e32 v87, s27, v200
	v_alignbit_b32 v86, v86, v87, 31
	v_subrev_u32_e32 v87, s27, v201
	v_alignbit_b32 v86, v86, v87, 31
	v_subrev_u32_e32 v87, s27, v202
	v_alignbit_b32 v86, v86, v87, 31
	v_subrev_u32_e32 v87, s27, v203
	v_alignbit_b32 v86, v86, v87, 31
	v_subrev_u32_e32 v87, s27, v204
	v_alignbit_b32 v86, v86, v87, 31
	v_subrev_u32_e32 v87, s27, v205
	v_alignbit_b32 v86, v86, v87, 31
	v_subrev_u32_e32 v87, s27, v206
	v_alignbit_b32 v86, v86, v87, 31
	v_subrev_u32_e32 v87, s27, v207
	v_alignbit_b32 v86, v86, v87, 31
	v_subrev_u32_e32 v87, s27, v208
	v_alignbit_b32 v86, v86, v87, 31
	v_subrev_u32_e32 v87, s27, v209
	v_alignbit_b32 v86, v86, v87, 31
	v_subrev_u32_e32 v87, s27, v210
	v_alignbit_b32 v86, v86, v87, 31
	v_subrev_u32_e32 v87, s27, v211
	v_alignbit_b32 v86, v86, v87, 31
	v_subrev_u32_e32 v87, s27, v212
	v_alignbit_b32 v86, v86, v87, 31
	v_subrev_u32_e32 v87, s27, v213
	v_alignbit_b32 v86, v86, v87, 31
	v_subrev_u32_e32 v87, s27, v214
	v_alignbit_b32 v86, v86, v87, 31
	v_subrev_u32_e32 v87, s27, v215
	v_alignbit_b32 v86, v86, v87, 31
	v_subrev_u32_e32 v87, s27, v216
	v_alignbit_b32 v86, v86, v87, 31
	v_subrev_u32_e32 v87, s27, v217
	v_alignbit_b32 v86, v86, v87, 31
	v_subrev_u32_e32 v87, s27, v218
	v_alignbit_b32 v86, v86, v87, 31
	v_subrev_u32_e32 v87, s27, v219
	v_alignbit_b32 v86, v86, v87, 31
	v_subrev_u32_e32 v87, s27, v220
	v_alignbit_b32 v86, v86, v87, 31
	v_subrev_u32_e32 v87, s27, v221
	v_alignbit_b32 v86, v86, v87, 31
	v_subrev_u32_e32 v87, s27, v222
	v_alignbit_b32 v86, v86, v87, 31
	v_subrev_u32_e32 v87, s27, v223
	v_alignbit_b32 v86, v86, v87, 31
	v_subrev_u32_e32 v87, s27, v224
	v_alignbit_b32 v86, v86, v87, 31
	v_subrev_u32_e32 v87, s27, v225
	v_alignbit_b32 v86, v86, v87, 31
	v_subrev_u32_e32 v87, s27, v226
	v_alignbit_b32 v86, v86, v87, 31
	v_subrev_u32_e32 v87, s27, v227
	v_alignbit_b32 v86, v86, v87, 31
	v_subrev_u32_e32 v87, s27, v228
	v_alignbit_b32 v86, v86, v87, 31
	v_subrev_u32_e32 v87, s27, v229
	v_alignbit_b32 v86, v86, v87, 31
	v_subrev_u32_e32 v87, s27, v230
	v_alignbit_b32 v86, v86, v87, 31
	v_subrev_u32_e32 v87, s27, v231
	v_alignbit_b32 v86, v86, v87, 31
	v_bcnt_u32_b32 v86, v86, 0
	s_nop 1
	v_add_u32_dpp v86, v86, v86 quad_perm:[1,0,3,2] row_mask:0xf bank_mask:0xf
	s_nop 1
	v_add_u32_dpp v86, v86, v86 quad_perm:[2,3,0,1] row_mask:0xf bank_mask:0xf
	s_nop 1
	v_add_u32_dpp v86, v86, v86 row_ror:4 row_mask:0xf bank_mask:0xf
	s_nop 1
	v_add_u32_dpp v86, v86, v86 row_ror:8 row_mask:0xf bank_mask:0xf
	s_nop 1
	v_add_u32_dpp v86, v86, v86 row_bcast:15 row_mask:0xa bank_mask:0xf
	s_nop 1
	v_add_u32_dpp v86, v86, v86 row_bcast:31 row_mask:0xc bank_mask:0xf
	s_nop 1
	v_readlane_b32 s12, v86, 63
	s_sub_i32 s12, 0x800, s12
	s_cmpk_ge_u32 s12, 0x100
	s_cselect_b32 s28, s27, s28
	s_cmpk_eq_u32 s12, 0x100
	s_cbranch_scc1 .Lp4s_705_done
	s_add_i32 s26, s26, -1
	s_cmp_ge_i32 s26, 0
	s_cbranch_scc1 .LBB0_705
.Lp4s_705_done:
	s_or_b32 s28, s28, s29
	v_mov_b32_e32 v66, s28
	s_branch .LBB0_712

; template <int NVM> __device__ __forceinline__ int cnt_ge(const unsigned (&key)[32], unsigned cand) {
;     unsigned c0 = 0, c1 = 0, c2 = 0, c3 = 0;
; #pragma unroll
;     for (int i = 0; i < NVM; i += 4) {
;         asm("v_cmp_ge_u32 vcc, %1, %2\n\tv_addc_co_u32 %0, vcc, 0, %0, vcc" : "+v"(c0) : "v"(key[i]), "v"(cand) : "vcc");
;         asm("v_cmp_ge_u32 vcc, %1, %2\n\tv_addc_co_u32 %0, vcc, 0, %0, vcc" : "+v"(c1) : "v"(key[i + 1]), "v"(cand) : "vcc");
;         asm("v_cmp_ge_u32 vcc, %1, %2\n\tv_addc_co_u32 %0, vcc, 0, %0, vcc" : "+v"(c2) : "v"(key[i + 2]), "v"(cand) : "vcc");
;         asm("v_cmp_ge_u32 vcc, %1, %2\n\tv_addc_co_u32 %0, vcc, 0, %0, vcc" : "+v"(c3) : "v"(key[i + 3]), "v"(cand) : "vcc"); }
;     const unsigned c = (c0 + c1) + (c2 + c3);
;     int tot = 0;
; #pragma unroll
;     for (int b = 0; b < 6; ++b) tot += __builtin_popcountll(__ballot((c >> b) & 1u)) << b;
;     return tot;
; }
; template <int NVM> __device__ __forceinline__ unsigned sel_thr(const unsigned (&key)[32]) {
;     unsigned Tt = 0u;
;     ...
;         if (cnt >= TOPK) { Tt = cand; if (cnt == TOPK) break; } }
;     return Tt;
; }
.LBB0_709:
	s_cbranch_execz .LBB0_712
	v_mov_b32_e32 v77, 31
	v_mov_b32_e32 v66, 0
	v_mov_b32_e32 v79, 0
	v_alignbit_b32 v79, v79, v5, 31
	v_alignbit_b32 v79, v79, v36, 31
	v_alignbit_b32 v79, v79, v39, 31
	v_alignbit_b32 v79, v79, v37, 31
	v_alignbit_b32 v79, v79, v38, 31
	v_alignbit_b32 v79, v79, v67, 31
	v_alignbit_b32 v79, v79, v43, 31
	v_alignbit_b32 v79, v79, v68, 31
	v_alignbit_b32 v79, v79, v69, 31
	v_alignbit_b32 v79, v79, v70, 31
	v_alignbit_b32 v79, v79, v73, 31
	v_alignbit_b32 v79, v79, v71, 31
	v_alignbit_b32 v79, v79, v72, 31
	v_alignbit_b32 v79, v79, v74, 31
	v_alignbit_b32 v79, v79, v52, 31
	v_alignbit_b32 v79, v79, v75, 31
	v_alignbit_b32 v79, v79, v76, 31
	v_alignbit_b32 v79, v79, v50, 31
	v_alignbit_b32 v79, v79, v54, 31
	v_alignbit_b32 v79, v79, v51, 31
	v_alignbit_b32 v79, v79, v53, 31
	v_alignbit_b32 v79, v79, v55, 31
	v_alignbit_b32 v79, v79, v56, 31
	v_alignbit_b32 v79, v79, v57, 31
	v_bcnt_u32_b32 v79, v79, 0
	s_nop 1
	v_add_u32_dpp v79, v79, v79 quad_perm:[1,0,3,2] row_mask:0xf bank_mask:0xf
	s_nop 1
	v_add_u32_dpp v79, v79, v79 quad_perm:[2,3,0,1] row_mask:0xf bank_mask:0xf
	s_nop 1
	v_add_u32_dpp v79, v79, v79 row_ror:4 row_mask:0xf bank_mask:0xf
	s_nop 1
	v_add_u32_dpp v79, v79, v79 row_ror:8 row_mask:0xf bank_mask:0xf
	s_nop 1
	v_add_u32_dpp v79, v79, v79 row_bcast:15 row_mask:0xa bank_mask:0xf
	s_nop 1
	v_add_u32_dpp v79, v79, v79 row_bcast:31 row_mask:0xc bank_mask:0xf
	s_nop 1
	v_readlane_b32 s12, v79, 63
	s_mov_b32 s28, 0
	s_mov_b32 s29, 0
	s_cmpk_lt_u32 s12, 0x100
	s_cbranch_scc1 .Lp4s_711_lo
	s_mov_b32 s29, 0x80000000
	s_cmpk_eq_u32 s12, 0x100
	s_cbranch_scc1 .Lp4s_711_done
	v_ashrrev_i32_e32 v81, 31, v5
	v_and_b32_e32 v82, 0x7fffffff, v5
	v_and_b32_e32 v200, v81, v82
	v_ashrrev_i32_e32 v81, 31, v36
	v_and_b32_e32 v82, 0x7fffffff, v36
	v_and_b32_e32 v201, v81, v82
	v_ashrrev_i32_e32 v81, 31, v39
	v_and_b32_e32 v82, 0x7fffffff, v39
	v_and_b32_e32 v202, v81, v82
	v_ashrrev_i32_e32 v81, 31, v37
	v_and_b32_e32 v82, 0x7fffffff, v37
	v_and_b32_e32 v203, v81, v82
	v_ashrrev_i32_e32 v81, 31, v38
	v_and_b32_e32 v82, 0x7fffffff, v38
	v_and_b32_e32 v204, v81, v82
	v_ashrrev_i32_e32 v81, 31, v67
	v_and_b32_e32 v82, 0x7fffffff, v67
	v_and_b32_e32 v205, v81, v82
	v_ashrrev_i32_e32 v81, 31, v43
	v_and_b32_e32 v82, 0x7fffffff, v43
	v_and_b32_e32 v206, v81, v82
	v_ashrrev_i32_e32 v81, 31, v68
	v_and_b32_e32 v82, 0x7fffffff, v68
	v_and_b32_e32 v207, v81, v82
	v_ashrrev_i32_e32 v81, 31, v69
	v_and_b32_e32 v82, 0x7fffffff, v69
	v_and_b32_e32 v208, v81, v82
	v_ashrrev_i32_e32 v81, 31, v70
	v_and_b32_e32 v82, 0x7fffffff, v70
	v_and_b32_e32 v209, v81, v82
	v_ashrrev_i32_e32 v81, 31, v73
	v_and_b32_e32 v82, 0x7fffffff, v73
	v_and_b32_e32 v210, v81, v82
	v_ashrrev_i32_e32 v81, 31, v71
	v_and_b32_e32 v82, 0x7fffffff, v71
	v_and_b32_e32 v211, v81, v82
	v_ashrrev_i32_e32 v81, 31, v72
	v_and_b32_e32 v82, 0x7fffffff, v72
	v_and_b32_e32 v212, v81, v82
	v_ashrrev_i32_e32 v81, 31, v74
	v_and_b32_e32 v82, 0x7fffffff, v74
	v_and_b32_e32 v213, v81, v82
	v_ashrrev_i32_e32 v81, 31, v52
	v_and_b32_e32 v82, 0x7fffffff, v52
	v_and_b32_e32 v214, v81, v82
	v_ashrrev_i32_e32 v81, 31, v75
	v_and_b32_e32 v82, 0x7fffffff, v75
	v_and_b32_e32 v215, v81, v82
	v_ashrrev_i32_e32 v81, 31, v76
	v_and_b32_e32 v82, 0x7fffffff, v76
	v_and_b32_e32 v216, v81, v82
	v_ashrrev_i32_e32 v81, 31, v50
	v_and_b32_e32 v82, 0x7fffffff, v50
	v_and_b32_e32 v217, v81, v82
	v_ashrrev_i32_e32 v81, 31, v54
	v_and_b32_e32 v82, 0x7fffffff, v54
	v_and_b32_e32 v218, v81, v82
	v_ashrrev_i32_e32 v81, 31, v51
	v_and_b32_e32 v82, 0x7fffffff, v51
	v_and_b32_e32 v219, v81, v82
	v_ashrrev_i32_e32 v81, 31, v53
	v_and_b32_e32 v82, 0x7fffffff, v53
	v_and_b32_e32 v220, v81, v82
	v_ashrrev_i32_e32 v81, 31, v55
	v_and_b32_e32 v82, 0x7fffffff, v55
	v_and_b32_e32 v221, v81, v82
	v_ashrrev_i32_e32 v81, 31, v56
	v_and_b32_e32 v82, 0x7fffffff, v56
	v_and_b32_e32 v222, v81, v82
	v_ashrrev_i32_e32 v81, 31, v57
	v_and_b32_e32 v82, 0x7fffffff, v57
	v_and_b32_e32 v223, v81, v82
	s_branch .Lp4s_711_go
.Lp4s_711_lo:
	v_ashrrev_i32_e32 v81, 31, v5
	v_or_b32_e32 v82, v81, v5
	v_and_b32_e32 v200, 0x7fffffff, v82
	v_ashrrev_i32_e32 v81, 31, v36
	v_or_b32_e32 v82, v81, v36
	v_and_b32_e32 v201, 0x7fffffff, v82
	v_ashrrev_i32_e32 v81, 31, v39
	v_or_b32_e32 v82, v81, v39
	v_and_b32_e32 v202, 0x7fffffff, v82
	v_ashrrev_i32_e32 v81, 31, v37
	v_or_b32_e32 v82, v81, v37
	v_and_b32_e32 v203, 0x7fffffff, v82
	v_ashrrev_i32_e32 v81, 31, v38
	v_or_b32_e32 v82, v81, v38
	v_and_b32_e32 v204, 0x7fffffff, v82
	v_ashrrev_i32_e32 v81, 31, v67
	v_or_b32_e32 v82, v81, v67
	v_and_b32_e32 v205, 0x7fffffff, v82
	v_ashrrev_i32_e32 v81, 31, v43
	v_or_b32_e32 v82, v81, v43
	v_and_b32_e32 v206, 0x7fffffff, v82
	v_ashrrev_i32_e32 v81, 31, v68
	v_or_b32_e32 v82, v81, v68
	v_and_b32_e32 v207, 0x7fffffff, v82
	v_ashrrev_i32_e32 v81, 31, v69
	v_or_b32_e32 v82, v81, v69
	v_and_b32_e32 v208, 0x7fffffff, v82
	v_ashrrev_i32_e32 v81, 31, v70
	v_or_b32_e32 v82, v81, v70
	v_and_b32_e32 v209, 0x7fffffff, v82
	v_ashrrev_i32_e32 v81, 31, v73
	v_or_b32_e32 v82, v81, v73
	v_and_b32_e32 v210, 0x7fffffff, v82
	v_ashrrev_i32_e32 v81, 31, v71
	v_or_b32_e32 v82, v81, v71
	v_and_b32_e32 v211, 0x7fffffff, v82
	v_ashrrev_i32_e32 v81, 31, v72
	v_or_b32_e32 v82, v81, v72
	v_and_b32_e32 v212, 0x7fffffff, v82
	v_ashrrev_i32_e32 v81, 31, v74
	v_or_b32_e32 v82, v81, v74
	v_and_b32_e32 v213, 0x7fffffff, v82
	v_ashrrev_i32_e32 v81, 31, v52
	v_or_b32_e32 v82, v81, v52
	v_and_b32_e32 v214, 0x7fffffff, v82
	v_ashrrev_i32_e32 v81, 31, v75
	v_or_b32_e32 v82, v81, v75
	v_and_b32_e32 v215, 0x7fffffff, v82
	v_ashrrev_i32_e32 v81, 31, v76
	v_or_b32_e32 v82, v81, v76
	v_and_b32_e32 v216, 0x7fffffff, v82
	v_ashrrev_i32_e32 v81, 31, v50
	v_or_b32_e32 v82, v81, v50
	v_and_b32_e32 v217, 0x7fffffff, v82
	v_ashrrev_i32_e32 v81, 31, v54
	v_or_b32_e32 v82, v81, v54
	v_and_b32_e32 v218, 0x7fffffff, v82
	v_ashrrev_i32_e32 v81, 31, v51
	v_or_b32_e32 v82, v81, v51
	v_and_b32_e32 v219, 0x7fffffff, v82
	v_ashrrev_i32_e32 v81, 31, v53
	v_or_b32_e32 v82, v81, v53
	v_and_b32_e32 v220, 0x7fffffff, v82
	v_ashrrev_i32_e32 v81, 31, v55
	v_or_b32_e32 v82, v81, v55
	v_and_b32_e32 v221, 0x7fffffff, v82
	v_ashrrev_i32_e32 v81, 31, v56
	v_or_b32_e32 v82, v81, v56
	v_and_b32_e32 v222, 0x7fffffff, v82
	v_ashrrev_i32_e32 v81, 31, v57
	v_or_b32_e32 v82, v81, v57
	v_and_b32_e32 v223, 0x7fffffff, v82

; template <int NVM> __device__ __forceinline__ int cnt_ge(const unsigned (&key)[32], unsigned cand) {
;     unsigned c0 = 0, c1 = 0, c2 = 0, c3 = 0;
; #pragma unroll
;     for (int i = 0; i < NVM; i += 4) {
;         asm("v_cmp_ge_u32 vcc, %1, %2\n\tv_addc_co_u32 %0, vcc, 0, %0, vcc" : "+v"(c0) : "v"(key[i]), "v"(cand) : "vcc");
;         asm("v_cmp_ge_u32 vcc, %1, %2\n\tv_addc_co_u32 %0, vcc, 0, %0, vcc" : "+v"(c1) : "v"(key[i + 1]), "v"(cand) : "vcc");
;         asm("v_cmp_ge_u32 vcc, %1, %2\n\tv_addc_co_u32 %0, vcc, 0, %0, vcc" : "+v"(c2) : "v"(key[i + 2]), "v"(cand) : "vcc");
;         asm("v_cmp_ge_u32 vcc, %1, %2\n\tv_addc_co_u32 %0, vcc, 0, %0, vcc" : "+v"(c3) : "v"(key[i + 3]), "v"(cand) : "vcc"); }
;     const unsigned c = (c0 + c1) + (c2 + c3);
;     int tot = 0;
; #pragma unroll
;     for (int b = 0; b < 6; ++b) tot += __builtin_popcountll(__ballot((c >> b) & 1u)) << b;
;     return tot;
; }
; template <int NVM> __device__ __forceinline__ unsigned sel_thr(const unsigned (&key)[32]) {
;     unsigned Tt = 0u;
;     ...
;         if (cnt >= TOPK) { Tt = cand; if (cnt == TOPK) break; } }
;     return Tt;
; }
.LBB0_711:
	s_lshl_b32 s27, 1, s26
	s_or_b32 s27, s27, s28
	v_mov_b32_e32 v79, 0
	v_subrev_u32_e32 v80, s27, v200
	v_alignbit_b32 v79, v79, v80, 31
	v_subrev_u32_e32 v80, s27, v201
	v_alignbit_b32 v79, v79, v80, 31
	v_subrev_u32_e32 v80, s27, v202
	v_alignbit_b32 v79, v79, v80, 31
	v_subrev_u32_e32 v80, s27, v203
	v_alignbit_b32 v79, v79, v80, 31
	v_subrev_u32_e32 v80, s27, v204
	v_alignbit_b32 v79, v79, v80, 31
	v_subrev_u32_e32 v80, s27, v205
	v_alignbit_b32 v79, v79, v80, 31
	v_subrev_u32_e32 v80, s27, v206
	v_alignbit_b32 v79, v79, v80, 31
	v_subrev_u32_e32 v80, s27, v207
	v_alignbit_b32 v79, v79, v80, 31
	v_subrev_u32_e32 v80, s27, v208
	v_alignbit_b32 v79, v79, v80, 31
	v_subrev_u32_e32 v80, s27, v209
	v_alignbit_b32 v79, v79, v80, 31
	v_subrev_u32_e32 v80, s27, v210
	v_alignbit_b32 v79, v79, v80, 31
	v_subrev_u32_e32 v80, s27, v211
	v_alignbit_b32 v79, v79, v80, 31
	v_subrev_u32_e32 v80, s27, v212
	v_alignbit_b32 v79, v79, v80, 31
	v_subrev_u32_e32 v80, s27, v213
	v_alignbit_b32 v79, v79, v80, 31
	v_subrev_u32_e32 v80, s27, v214
	v_alignbit_b32 v79, v79, v80, 31
	v_subrev_u32_e32 v80, s27, v215
	v_alignbit_b32 v79, v79, v80, 31
	v_subrev_u32_e32 v80, s27, v216
	v_alignbit_b32 v79, v79, v80, 31
	v_subrev_u32_e32 v80, s27, v217
	v_alignbit_b32 v79, v79, v80, 31
	v_subrev_u32_e32 v80, s27, v218
	v_alignbit_b32 v79, v79, v80, 31
	v_subrev_u32_e32 v80, s27, v219
	v_alignbit_b32 v79, v79, v80, 31
	v_subrev_u32_e32 v80, s27, v220
	v_alignbit_b32 v79, v79, v80, 31
	v_subrev_u32_e32 v80, s27, v221
	v_alignbit_b32 v79, v79, v80, 31
	v_subrev_u32_e32 v80, s27, v222
	v_alignbit_b32 v79, v79, v80, 31
	v_subrev_u32_e32 v80, s27, v223
	v_alignbit_b32 v79, v79, v80, 31
	v_bcnt_u32_b32 v79, v79, 0
	s_nop 1
	v_add_u32_dpp v79, v79, v79 quad_perm:[1,0,3,2] row_mask:0xf bank_mask:0xf
	s_nop 1
	v_add_u32_dpp v79, v79, v79 quad_perm:[2,3,0,1] row_mask:0xf bank_mask:0xf
	s_nop 1
	v_add_u32_dpp v79, v79, v79 row_ror:4 row_mask:0xf bank_mask:0xf
	s_nop 1
	v_add_u32_dpp v79, v79, v79 row_ror:8 row_mask:0xf bank_mask:0xf
	s_nop 1
	v_add_u32_dpp v79, v79, v79 row_bcast:15 row_mask:0xa bank_mask:0xf
	s_nop 1
	v_add_u32_dpp v79, v79, v79 row_bcast:31 row_mask:0xc bank_mask:0xf
	s_nop 1
	v_readlane_b32 s12, v79, 63
	s_sub_i32 s12, 0x600, s12
	s_cmpk_ge_u32 s12, 0x100
	s_cselect_b32 s28, s27, s28
	s_cmpk_eq_u32 s12, 0x100
	s_cbranch_scc1 .Lp4s_711_done
	s_add_i32 s26, s26, -1
	s_cmp_ge_i32 s26, 0
	s_cbranch_scc1 .LBB0_711
.Lp4s_711_done:
	s_or_b32 s28, s28, s29
	v_mov_b32_e32 v66, s28

; template <int NVM> __device__ __forceinline__ int cnt_ge(const unsigned (&key)[32], unsigned cand) {
;     unsigned c0 = 0, c1 = 0, c2 = 0, c3 = 0;
; #pragma unroll
;     for (int i = 0; i < NVM; i += 4) {
;         asm("v_cmp_ge_u32 vcc, %1, %2\n\tv_addc_co_u32 %0, vcc, 0, %0, vcc" : "+v"(c0) : "v"(key[i]), "v"(cand) : "vcc");
;         asm("v_cmp_ge_u32 vcc, %1, %2\n\tv_addc_co_u32 %0, vcc, 0, %0, vcc" : "+v"(c1) : "v"(key[i + 1]), "v"(cand) : "vcc");
;         asm("v_cmp_ge_u32 vcc, %1, %2\n\tv_addc_co_u32 %0, vcc, 0, %0, vcc" : "+v"(c2) : "v"(key[i + 2]), "v"(cand) : "vcc");
;         asm("v_cmp_ge_u32 vcc, %1, %2\n\tv_addc_co_u32 %0, vcc, 0, %0, vcc" : "+v"(c3) : "v"(key[i + 3]), "v"(cand) : "vcc"); }
;     const unsigned c = (c0 + c1) + (c2 + c3);
;     int tot = 0;
; #pragma unroll
;     for (int b = 0; b < 6; ++b) tot += __builtin_popcountll(__ballot((c >> b) & 1u)) << b;
;     return tot;
; }
; template <int NVM> __device__ __forceinline__ unsigned sel_thr(const unsigned (&key)[32]) {
;     unsigned Tt = 0u;
;     ...
;         if (cnt >= TOPK) { Tt = cand; if (cnt == TOPK) break; } }
;     return Tt;
; }
.LBB0_713:
	v_mov_b32_e32 v70, 31
	v_mov_b32_e32 v66, 0
	v_mov_b32_e32 v72, 0
	v_alignbit_b32 v72, v72, v5, 31
	v_alignbit_b32 v72, v72, v36, 31
	v_alignbit_b32 v72, v72, v39, 31
	v_alignbit_b32 v72, v72, v37, 31
	v_alignbit_b32 v72, v72, v38, 31
	v_alignbit_b32 v72, v72, v67, 31
	v_alignbit_b32 v72, v72, v43, 31
	v_alignbit_b32 v72, v72, v68, 31
	v_alignbit_b32 v72, v72, v69, 31
	v_alignbit_b32 v72, v72, v42, 31
	v_alignbit_b32 v72, v72, v46, 31
	v_alignbit_b32 v72, v72, v44, 31
	v_alignbit_b32 v72, v72, v45, 31
	v_alignbit_b32 v72, v72, v47, 31
	v_alignbit_b32 v72, v72, v48, 31
	v_alignbit_b32 v72, v72, v49, 31
	v_bcnt_u32_b32 v72, v72, 0
	s_nop 1
	v_add_u32_dpp v72, v72, v72 quad_perm:[1,0,3,2] row_mask:0xf bank_mask:0xf
	s_nop 1
	v_add_u32_dpp v72, v72, v72 quad_perm:[2,3,0,1] row_mask:0xf bank_mask:0xf
	s_nop 1
	v_add_u32_dpp v72, v72, v72 row_ror:4 row_mask:0xf bank_mask:0xf
	s_nop 1
	v_add_u32_dpp v72, v72, v72 row_ror:8 row_mask:0xf bank_mask:0xf
	s_nop 1
	v_add_u32_dpp v72, v72, v72 row_bcast:15 row_mask:0xa bank_mask:0xf
	s_nop 1
	v_add_u32_dpp v72, v72, v72 row_bcast:31 row_mask:0xc bank_mask:0xf
	s_nop 1
	v_readlane_b32 s12, v72, 63
	s_mov_b32 s28, 0
	s_mov_b32 s29, 0
	s_cmpk_lt_u32 s12, 0x100
	s_cbranch_scc1 .Lp4s_714_lo
	s_mov_b32 s29, 0x80000000
	s_cmpk_eq_u32 s12, 0x100
	s_cbranch_scc1 .Lp4s_714_done
	v_ashrrev_i32_e32 v74, 31, v5
	v_and_b32_e32 v75, 0x7fffffff, v5
	v_and_b32_e32 v200, v74, v75
	v_ashrrev_i32_e32 v74, 31, v36
	v_and_b32_e32 v75, 0x7fffffff, v36
	v_and_b32_e32 v201, v74, v75
	v_ashrrev_i32_e32 v74, 31, v39
	v_and_b32_e32 v75, 0x7fffffff, v39
	v_and_b32_e32 v202, v74, v75
	v_ashrrev_i32_e32 v74, 31, v37
	v_and_b32_e32 v75, 0x7fffffff, v37
	v_and_b32_e32 v203, v74, v75
	v_ashrrev_i32_e32 v74, 31, v38
	v_and_b32_e32 v75, 0x7fffffff, v38
	v_and_b32_e32 v204, v74, v75
	v_ashrrev_i32_e32 v74, 31, v67
	v_and_b32_e32 v75, 0x7fffffff, v67
	v_and_b32_e32 v205, v74, v75
	v_ashrrev_i32_e32 v74, 31, v43
	v_and_b32_e32 v75, 0x7fffffff, v43
	v_and_b32_e32 v206, v74, v75
	v_ashrrev_i32_e32 v74, 31, v68
	v_and_b32_e32 v75, 0x7fffffff, v68
	v_and_b32_e32 v207, v74, v75
	v_ashrrev_i32_e32 v74, 31, v69
	v_and_b32_e32 v75, 0x7fffffff, v69
	v_and_b32_e32 v208, v74, v75
	v_ashrrev_i32_e32 v74, 31, v42
	v_and_b32_e32 v75, 0x7fffffff, v42
	v_and_b32_e32 v209, v74, v75
	v_ashrrev_i32_e32 v74, 31, v46
	v_and_b32_e32 v75, 0x7fffffff, v46
	v_and_b32_e32 v210, v74, v75
	v_ashrrev_i32_e32 v74, 31, v44
	v_and_b32_e32 v75, 0x7fffffff, v44
	v_and_b32_e32 v211, v74, v75
	v_ashrrev_i32_e32 v74, 31, v45
	v_and_b32_e32 v75, 0x7fffffff, v45
	v_and_b32_e32 v212, v74, v75
	v_ashrrev_i32_e32 v74, 31, v47
	v_and_b32_e32 v75, 0x7fffffff, v47
	v_and_b32_e32 v213, v74, v75
	v_ashrrev_i32_e32 v74, 31, v48
	v_and_b32_e32 v75, 0x7fffffff, v48
	v_and_b32_e32 v214, v74, v75
	v_ashrrev_i32_e32 v74, 31, v49
	v_and_b32_e32 v75, 0x7fffffff, v49
	v_and_b32_e32 v215, v74, v75
	s_branch .Lp4s_714_go
.Lp4s_714_lo:
	v_ashrrev_i32_e32 v74, 31, v5
	v_or_b32_e32 v75, v74, v5
	v_and_b32_e32 v200, 0x7fffffff, v75
	v_ashrrev_i32_e32 v74, 31, v36
	v_or_b32_e32 v75, v74, v36
	v_and_b32_e32 v201, 0x7fffffff, v75
	v_ashrrev_i32_e32 v74, 31, v39
	v_or_b32_e32 v75, v74, v39
	v_and_b32_e32 v202, 0x7fffffff, v75
	v_ashrrev_i32_e32 v74, 31, v37
	v_or_b32_e32 v75, v74, v37
	v_and_b32_e32 v203, 0x7fffffff, v75
	v_ashrrev_i32_e32 v74, 31, v38
	v_or_b32_e32 v75, v74, v38
	v_and_b32_e32 v204, 0x7fffffff, v75
	v_ashrrev_i32_e32 v74, 31, v67
	v_or_b32_e32 v75, v74, v67
	v_and_b32_e32 v205, 0x7fffffff, v75
	v_ashrrev_i32_e32 v74, 31, v43
	v_or_b32_e32 v75, v74, v43
	v_and_b32_e32 v206, 0x7fffffff, v75
	v_ashrrev_i32_e32 v74, 31, v68
	v_or_b32_e32 v75, v74, v68
	v_and_b32_e32 v207, 0x7fffffff, v75
	v_ashrrev_i32_e32 v74, 31, v69
	v_or_b32_e32 v75, v74, v69
	v_and_b32_e32 v208, 0x7fffffff, v75
	v_ashrrev_i32_e32 v74, 31, v42
	v_or_b32_e32 v75, v74, v42
	v_and_b32_e32 v209, 0x7fffffff, v75
	v_ashrrev_i32_e32 v74, 31, v46
	v_or_b32_e32 v75, v74, v46
	v_and_b32_e32 v210, 0x7fffffff, v75
	v_ashrrev_i32_e32 v74, 31, v44
	v_or_b32_e32 v75, v74, v44
	v_and_b32_e32 v211, 0x7fffffff, v75
	v_ashrrev_i32_e32 v74, 31, v45
	v_or_b32_e32 v75, v74, v45
	v_and_b32_e32 v212, 0x7fffffff, v75
	v_ashrrev_i32_e32 v74, 31, v47
	v_or_b32_e32 v75, v74, v47
	v_and_b32_e32 v213, 0x7fffffff, v75
	v_ashrrev_i32_e32 v74, 31, v48
	v_or_b32_e32 v75, v74, v48
	v_and_b32_e32 v214, 0x7fffffff, v75
	v_ashrrev_i32_e32 v74, 31, v49
	v_or_b32_e32 v75, v74, v49
	v_and_b32_e32 v215, 0x7fffffff, v75

; template <int NVM> __device__ __forceinline__ int cnt_ge(const unsigned (&key)[32], unsigned cand) {
;     unsigned c0 = 0, c1 = 0, c2 = 0, c3 = 0;
; #pragma unroll
;     for (int i = 0; i < NVM; i += 4) {
;         asm("v_cmp_ge_u32 vcc, %1, %2\n\tv_addc_co_u32 %0, vcc, 0, %0, vcc" : "+v"(c0) : "v"(key[i]), "v"(cand) : "vcc");
;         asm("v_cmp_ge_u32 vcc, %1, %2\n\tv_addc_co_u32 %0, vcc, 0, %0, vcc" : "+v"(c1) : "v"(key[i + 1]), "v"(cand) : "vcc");
;         asm("v_cmp_ge_u32 vcc, %1, %2\n\tv_addc_co_u32 %0, vcc, 0, %0, vcc" : "+v"(c2) : "v"(key[i + 2]), "v"(cand) : "vcc");
;         asm("v_cmp_ge_u32 vcc, %1, %2\n\tv_addc_co_u32 %0, vcc, 0, %0, vcc" : "+v"(c3) : "v"(key[i + 3]), "v"(cand) : "vcc"); }
;     const unsigned c = (c0 + c1) + (c2 + c3);
;     int tot = 0;
; #pragma unroll
;     for (int b = 0; b < 6; ++b) tot += __builtin_popcountll(__ballot((c >> b) & 1u)) << b;
;     return tot;
; }
; template <int NVM> __device__ __forceinline__ unsigned sel_thr(const unsigned (&key)[32]) {
;     unsigned Tt = 0u;
;     ...
;         if (cnt >= TOPK) { Tt = cand; if (cnt == TOPK) break; } }
;     return Tt;
; }
.LBB0_714:
	s_lshl_b32 s27, 1, s26
	s_or_b32 s27, s27, s28
	v_mov_b32_e32 v72, 0
	v_subrev_u32_e32 v73, s27, v200
	v_alignbit_b32 v72, v72, v73, 31
	v_subrev_u32_e32 v73, s27, v201
	v_alignbit_b32 v72, v72, v73, 31
	v_subrev_u32_e32 v73, s27, v202
	v_alignbit_b32 v72, v72, v73, 31
	v_subrev_u32_e32 v73, s27, v203
	v_alignbit_b32 v72, v72, v73, 31
	v_subrev_u32_e32 v73, s27, v204
	v_alignbit_b32 v72, v72, v73, 31
	v_subrev_u32_e32 v73, s27, v205
	v_alignbit_b32 v72, v72, v73, 31
	v_subrev_u32_e32 v73, s27, v206
	v_alignbit_b32 v72, v72, v73, 31
	v_subrev_u32_e32 v73, s27, v207
	v_alignbit_b32 v72, v72, v73, 31
	v_subrev_u32_e32 v73, s27, v208
	v_alignbit_b32 v72, v72, v73, 31
	v_subrev_u32_e32 v73, s27, v209
	v_alignbit_b32 v72, v72, v73, 31
	v_subrev_u32_e32 v73, s27, v210
	v_alignbit_b32 v72, v72, v73, 31
	v_subrev_u32_e32 v73, s27, v211
	v_alignbit_b32 v72, v72, v73, 31
	v_subrev_u32_e32 v73, s27, v212
	v_alignbit_b32 v72, v72, v73, 31
	v_subrev_u32_e32 v73, s27, v213
	v_alignbit_b32 v72, v72, v73, 31
	v_subrev_u32_e32 v73, s27, v214
	v_alignbit_b32 v72, v72, v73, 31
	v_subrev_u32_e32 v73, s27, v215
	v_alignbit_b32 v72, v72, v73, 31
	v_bcnt_u32_b32 v72, v72, 0
	s_nop 1
	v_add_u32_dpp v72, v72, v72 quad_perm:[1,0,3,2] row_mask:0xf bank_mask:0xf
	s_nop 1
	v_add_u32_dpp v72, v72, v72 quad_perm:[2,3,0,1] row_mask:0xf bank_mask:0xf
	s_nop 1
	v_add_u32_dpp v72, v72, v72 row_ror:4 row_mask:0xf bank_mask:0xf
	s_nop 1
	v_add_u32_dpp v72, v72, v72 row_ror:8 row_mask:0xf bank_mask:0xf
	s_nop 1
	v_add_u32_dpp v72, v72, v72 row_bcast:15 row_mask:0xa bank_mask:0xf
	s_nop 1
	v_add_u32_dpp v72, v72, v72 row_bcast:31 row_mask:0xc bank_mask:0xf
	s_nop 1
	v_readlane_b32 s12, v72, 63
	s_sub_i32 s12, 0x400, s12
	s_cmpk_ge_u32 s12, 0x100
	s_cselect_b32 s28, s27, s28
	s_cmpk_eq_u32 s12, 0x100
	s_cbranch_scc1 .Lp4s_714_done
	s_add_i32 s26, s26, -1
	s_cmp_ge_i32 s26, 0
	s_cbranch_scc1 .LBB0_714

; template <int NVM> __device__ __forceinline__ int cnt_ge(const unsigned (&key)[32], unsigned cand) {
;     unsigned c0 = 0, c1 = 0, c2 = 0, c3 = 0;
; #pragma unroll
;     for (int i = 0; i < NVM; i += 4) {
;         asm("v_cmp_ge_u32 vcc, %1, %2\n\tv_addc_co_u32 %0, vcc, 0, %0, vcc" : "+v"(c0) : "v"(key[i]), "v"(cand) : "vcc");
;         asm("v_cmp_ge_u32 vcc, %1, %2\n\tv_addc_co_u32 %0, vcc, 0, %0, vcc" : "+v"(c1) : "v"(key[i + 1]), "v"(cand) : "vcc");
;         asm("v_cmp_ge_u32 vcc, %1, %2\n\tv_addc_co_u32 %0, vcc, 0, %0, vcc" : "+v"(c2) : "v"(key[i + 2]), "v"(cand) : "vcc");
;         asm("v_cmp_ge_u32 vcc, %1, %2\n\tv_addc_co_u32 %0, vcc, 0, %0, vcc" : "+v"(c3) : "v"(key[i + 3]), "v"(cand) : "vcc"); }
;     const unsigned c = (c0 + c1) + (c2 + c3);
;     int tot = 0;
; #pragma unroll
;     for (int b = 0; b < 6; ++b) tot += __builtin_popcountll(__ballot((c >> b) & 1u)) << b;
;     return tot;
; }
; template <int NVM> __device__ __forceinline__ unsigned sel_thr(const unsigned (&key)[32]) {
;     unsigned Tt = 0u;
;     ...
;         if (cnt >= TOPK) { Tt = cand; if (cnt == TOPK) break; } }
;     return Tt;
; }
.LBB0_716:
	v_mov_b32_e32 v67, 31
	v_mov_b32_e32 v66, 0
	v_mov_b32_e32 v69, 0
	v_alignbit_b32 v69, v69, v5, 31
	v_alignbit_b32 v69, v69, v36, 31
	v_alignbit_b32 v69, v69, v39, 31
	v_alignbit_b32 v69, v69, v37, 31
	v_alignbit_b32 v69, v69, v38, 31
	v_alignbit_b32 v69, v69, v35, 31
	v_alignbit_b32 v69, v69, v40, 31
	v_alignbit_b32 v69, v69, v41, 31
	v_bcnt_u32_b32 v69, v69, 0
	s_nop 1
	v_add_u32_dpp v69, v69, v69 quad_perm:[1,0,3,2] row_mask:0xf bank_mask:0xf
	s_nop 1
	v_add_u32_dpp v69, v69, v69 quad_perm:[2,3,0,1] row_mask:0xf bank_mask:0xf
	s_nop 1
	v_add_u32_dpp v69, v69, v69 row_ror:4 row_mask:0xf bank_mask:0xf
	s_nop 1
	v_add_u32_dpp v69, v69, v69 row_ror:8 row_mask:0xf bank_mask:0xf
	s_nop 1
	v_add_u32_dpp v69, v69, v69 row_bcast:15 row_mask:0xa bank_mask:0xf
	s_nop 1
	v_add_u32_dpp v69, v69, v69 row_bcast:31 row_mask:0xc bank_mask:0xf
	s_nop 1
	v_readlane_b32 s12, v69, 63
	s_mov_b32 s28, 0
	s_mov_b32 s29, 0
	s_cmpk_lt_u32 s12, 0x100
	s_cbranch_scc1 .Lp4s_717_lo
	s_mov_b32 s29, 0x80000000
	s_cmpk_eq_u32 s12, 0x100
	s_cbranch_scc1 .Lp4s_717_done
	v_ashrrev_i32_e32 v71, 31, v5
	v_and_b32_e32 v72, 0x7fffffff, v5
	v_and_b32_e32 v200, v71, v72
	v_ashrrev_i32_e32 v71, 31, v36
	v_and_b32_e32 v72, 0x7fffffff, v36
	v_and_b32_e32 v201, v71, v72
	v_ashrrev_i32_e32 v71, 31, v39
	v_and_b32_e32 v72, 0x7fffffff, v39
	v_and_b32_e32 v202, v71, v72
	v_ashrrev_i32_e32 v71, 31, v37
	v_and_b32_e32 v72, 0x7fffffff, v37
	v_and_b32_e32 v203, v71, v72
	v_ashrrev_i32_e32 v71, 31, v38
	v_and_b32_e32 v72, 0x7fffffff, v38
	v_and_b32_e32 v204, v71, v72
	v_ashrrev_i32_e32 v71, 31, v35
	v_and_b32_e32 v72, 0x7fffffff, v35
	v_and_b32_e32 v205, v71, v72
	v_ashrrev_i32_e32 v71, 31, v40
	v_and_b32_e32 v72, 0x7fffffff, v40
	v_and_b32_e32 v206, v71, v72
	v_ashrrev_i32_e32 v71, 31, v41
	v_and_b32_e32 v72, 0x7fffffff, v41
	v_and_b32_e32 v207, v71, v72
	s_branch .Lp4s_717_go
.Lp4s_717_lo:
	v_ashrrev_i32_e32 v71, 31, v5
	v_or_b32_e32 v72, v71, v5
	v_and_b32_e32 v200, 0x7fffffff, v72
	v_ashrrev_i32_e32 v71, 31, v36
	v_or_b32_e32 v72, v71, v36
	v_and_b32_e32 v201, 0x7fffffff, v72
	v_ashrrev_i32_e32 v71, 31, v39
	v_or_b32_e32 v72, v71, v39
	v_and_b32_e32 v202, 0x7fffffff, v72
	v_ashrrev_i32_e32 v71, 31, v37
	v_or_b32_e32 v72, v71, v37
	v_and_b32_e32 v203, 0x7fffffff, v72
	v_ashrrev_i32_e32 v71, 31, v38
	v_or_b32_e32 v72, v71, v38
	v_and_b32_e32 v204, 0x7fffffff, v72
	v_ashrrev_i32_e32 v71, 31, v35
	v_or_b32_e32 v72, v71, v35
	v_and_b32_e32 v205, 0x7fffffff, v72
	v_ashrrev_i32_e32 v71, 31, v40
	v_or_b32_e32 v72, v71, v40
	v_and_b32_e32 v206, 0x7fffffff, v72
	v_ashrrev_i32_e32 v71, 31, v41
	v_or_b32_e32 v72, v71, v41
	v_and_b32_e32 v207, 0x7fffffff, v72

; template <int NVM> __device__ __forceinline__ int cnt_ge(const unsigned (&key)[32], unsigned cand) {
;     unsigned c0 = 0, c1 = 0, c2 = 0, c3 = 0;
; #pragma unroll
;     for (int i = 0; i < NVM; i += 4) {
;         asm("v_cmp_ge_u32 vcc, %1, %2\n\tv_addc_co_u32 %0, vcc, 0, %0, vcc" : "+v"(c0) : "v"(key[i]), "v"(cand) : "vcc");
;         asm("v_cmp_ge_u32 vcc, %1, %2\n\tv_addc_co_u32 %0, vcc, 0, %0, vcc" : "+v"(c1) : "v"(key[i + 1]), "v"(cand) : "vcc");
;         asm("v_cmp_ge_u32 vcc, %1, %2\n\tv_addc_co_u32 %0, vcc, 0, %0, vcc" : "+v"(c2) : "v"(key[i + 2]), "v"(cand) : "vcc");
;         asm("v_cmp_ge_u32 vcc, %1, %2\n\tv_addc_co_u32 %0, vcc, 0, %0, vcc" : "+v"(c3) : "v"(key[i + 3]), "v"(cand) : "vcc"); }
;     const unsigned c = (c0 + c1) + (c2 + c3);
;     int tot = 0;
; #pragma unroll
;     for (int b = 0; b < 6; ++b) tot += __builtin_popcountll(__ballot((c >> b) & 1u)) << b;
;     return tot;
; }
; template <int NVM> __device__ __forceinline__ unsigned sel_thr(const unsigned (&key)[32]) {
;     unsigned Tt = 0u;
;     ...
;         if (cnt >= TOPK) { Tt = cand; if (cnt == TOPK) break; } }
;     return Tt;
; }
.LBB0_717:
	s_lshl_b32 s27, 1, s26
	s_or_b32 s27, s27, s28
	v_mov_b32_e32 v69, 0
	v_subrev_u32_e32 v70, s27, v200
	v_alignbit_b32 v69, v69, v70, 31
	v_subrev_u32_e32 v70, s27, v201
	v_alignbit_b32 v69, v69, v70, 31
	v_subrev_u32_e32 v70, s27, v202
	v_alignbit_b32 v69, v69, v70, 31
	v_subrev_u32_e32 v70, s27, v203
	v_alignbit_b32 v69, v69, v70, 31
	v_subrev_u32_e32 v70, s27, v204
	v_alignbit_b32 v69, v69, v70, 31
	v_subrev_u32_e32 v70, s27, v205
	v_alignbit_b32 v69, v69, v70, 31
	v_subrev_u32_e32 v70, s27, v206
	v_alignbit_b32 v69, v69, v70, 31
	v_subrev_u32_e32 v70, s27, v207
	v_alignbit_b32 v69, v69, v70, 31
	v_bcnt_u32_b32 v69, v69, 0
	s_nop 1
	v_add_u32_dpp v69, v69, v69 quad_perm:[1,0,3,2] row_mask:0xf bank_mask:0xf
	s_nop 1
	v_add_u32_dpp v69, v69, v69 quad_perm:[2,3,0,1] row_mask:0xf bank_mask:0xf
	s_nop 1
	v_add_u32_dpp v69, v69, v69 row_ror:4 row_mask:0xf bank_mask:0xf
	s_nop 1
	v_add_u32_dpp v69, v69, v69 row_ror:8 row_mask:0xf bank_mask:0xf
	s_nop 1
	v_add_u32_dpp v69, v69, v69 row_bcast:15 row_mask:0xa bank_mask:0xf
	s_nop 1
	v_add_u32_dpp v69, v69, v69 row_bcast:31 row_mask:0xc bank_mask:0xf
	s_nop 1
	v_readlane_b32 s12, v69, 63
	s_sub_i32 s12, 0x200, s12
	s_cmpk_ge_u32 s12, 0x100
	s_cselect_b32 s28, s27, s28
	s_cmpk_eq_u32 s12, 0x100
	s_cbranch_scc1 .Lp4s_717_done
	s_add_i32 s26, s26, -1
	s_cmp_ge_i32 s26, 0
	s_cbranch_scc1 .LBB0_717
